# SGU LN batched + gating workgroups take 3 conversion entries (was 1) in the slack that frees
# speedup vs baseline: 1.0011x; 1.0011x over previous
;     int tid = threadIdx.x; asm volatile("" : "+v"(tid)); const int lane = tid & 63, wave = __builtin_amdgcn_readfirstlane(tid >> 6);
;     unsigned nxt = CQ_END; int left = quota;
; __global__ void __launch_bounds__(NWAVES * 64, 2) trunk_fwd(Args args) {
;     ...
;                 __syncthreads();
;                 conv_run(args.in[I_M1], args.in[I_M3], args.in[I_M2], MUP_T, MDN_T, ctl, MISC + 16, true, nullptr, 0u, 1);
.LBB0_301:
	v_mov_b32_e32 v2, v0
	s_waitcnt vmcnt(0)
	s_barrier
	v_mov_b32_e32 v127, 3
	v_readfirstlane_b32 s12, v2
	v_cmp_eq_u32_e64 s[0:1], 0, v2
	v_mov_b32_e32 v129, -1
	s_and_saveexec_b64 s[4:5], s[0:1]
	v_readlane_b32 s23, v255, 15
	s_cbranch_execz .LBB0_309
	s_mov_b64 s[8:9], exec
	v_mbcnt_lo_u32_b32 v3, s8, 0
	v_mbcnt_hi_u32_b32 v3, s9, v3
	v_cmp_eq_u32_e32 vcc, 0, v3
	s_and_saveexec_b64 s[6:7], vcc
	s_cbranch_execz .LBB0_304
	s_bcnt1_i32_b64 s8, s[8:9]
	v_mov_b32_e32 v4, s8
	v_readlane_b32 s8, v250, 18
	v_readlane_b32 s9, v250, 19
	s_nop 4
	global_atomic_add v4, v187, v4, s[8:9] sc0

.LBB0_308:
	s_or_b64 exec, exec, s[6:7]
	v_mov_b32_e32 v127, 2
